# speedup vs baseline: 1.0078x; 1.0078x over previous
attn_fwd_pwg4x64:
	s_load_dwordx2 s[22:23], s[0:1], 0x0
	s_load_dwordx8 s[4:11], s[0:1], 0x8
	s_load_dwordx2 s[36:37], s[0:1], 0x28
	s_load_dwordx4 s[16:19], s[0:1], 0x30
	s_load_dwordx2 s[20:21], s[0:1], 0x40
	s_and_b32 s3, s2, 15
	s_bfe_u32 s30, s2, 0x30004
	s_lshr_b32 s2, s2, 3
	s_and_b32 s2, s2, 0x1ffffff0
	s_or_b32 s2, s2, s3
	s_mov_b32 s3, 0
	s_lshl_b32 s31, s30, 8
	s_lshl_b64 s[26:27], s[2:3], 19
	s_lshl_b64 s[24:25], s[2:3], 11
	s_lshl_b64 s[38:39], s[2:3], 20
	s_lshl_b32 s43, s30, 17
	s_add_u32 s38, s38, s43
	s_addc_u32 s39, s39, 0
	v_and_b32_e32 v1, 15, v0
	v_lshrrev_b32_e32 v28, 4, v0
	v_lshrrev_b32_e32 v29, 6, v0
	v_lshlrev_b32_e32 v30, 5, v1
	v_lshl_or_b32 v2, v28, 9, v30
	v_bfe_u32 v31, v0, 4, 2
	v_lshl_or_b32 v3, v31, 9, v30
	v_lshl_or_b32 v3, v29, 15, v3
	v_lshlrev_b32_e32 v32, 4, v1
	v_lshl_or_b32 v26, v28, 8, v32
	s_lshl_b32 s43, s30, 16
	v_or_b32_e32 v26, s43, v26
	v_lshlrev_b32_e32 v38, 2, v0
	v_lshlrev_b32_e32 v40, 14, v29
	v_lshlrev_b32_e32 v33, 12, v29
	v_mbcnt_lo_u32_b32 v39, -1, 0
	v_mbcnt_hi_u32_b32 v39, -1, v39
	v_readfirstlane_b32 s28, v33
	v_readfirstlane_b32 s29, v33
	v_mov_b32_e32 v200, 0
	v_mov_b32_e32 v201, 0
	v_mov_b32_e32 v202, 0
	v_mov_b32_e32 v203, 0
	v_mov_b32_e32 v204, 0
	v_mov_b32_e32 v205, 0
	v_mov_b32_e32 v206, 0
	v_mov_b32_e32 v207, 0
	s_mov_b32 s44, 0x3e0293ee
	s_mov_b32 s45, 0x3e0293ee
	s_waitcnt lgkmcnt(0)
	s_add_u32 s12, s4, s26
	s_addc_u32 s13, s5, s27
	s_and_b32 s13, s13, 0xffff
	s_mov_b32 s14, 0x80000
	s_mov_b32 s15, 0x20000
	s_add_u32 s4, s6, s26
	s_addc_u32 s5, s7, s27
	s_and_b32 s5, s5, 0xffff
	s_mov_b32 s6, 0x80000
	s_mov_b32 s7, 0x20000
	s_add_u32 s32, s10, s38
	s_addc_u32 s33, s11, s39
	s_add_u32 s34, s36, s38
	s_addc_u32 s35, s37, s39
	s_lshl_b32 s43, s30, 17
	s_sub_u32 s80, s34, s43
	s_subb_u32 s81, s35, 0
	s_and_b32 s81, s81, 0xffff
	s_mov_b32 s82, 0x100000
	s_mov_b32 s83, 0x20000
	s_add_i32 s86, s43, 0x8000
	s_add_u32 s40, s22, s38
	s_addc_u32 s41, s23, s39
	s_lshl_b64 s[46:47], s[2:3], 5
	s_add_u32 s10, s16, s46
	s_addc_u32 s11, s17, s47
	s_lshl_b32 s43, s30, 2
	s_add_u32 s46, s10, s43
	s_addc_u32 s47, s11, 0
	s_lshl_b64 s[26:27], s[2:3], 12
	s_add_u32 s26, s18, s26
	s_addc_u32 s27, s19, s27
	s_lshl_b32 s43, s30, 9
	s_add_u32 s26, s26, s43
	s_addc_u32 s27, s27, 0
	global_load_dwordx4 v[42:45], v2, s[32:33] nt
	global_load_dwordx4 v[46:49], v2, s[32:33] offset:16 nt
	s_add_u32 s32, s32, 8192
	s_addc_u32 s33, s33, 0
	global_load_dwordx4 v[50:53], v2, s[32:33] nt
	global_load_dwordx4 v[54:57], v2, s[32:33] offset:16 nt
	s_add_u32 s32, s32, 8192
	s_addc_u32 s33, s33, 0
	global_load_dwordx4 v[68:71], v2, s[32:33] nt
	global_load_dwordx4 v[72:75], v2, s[32:33] offset:16 nt
	s_add_u32 s32, s32, 8192
	s_addc_u32 s33, s33, 0
	global_load_dwordx4 v[76:79], v2, s[32:33] nt
	global_load_dwordx4 v[80:83], v2, s[32:33] offset:16 nt
	s_add_u32 s32, s32, 8192
	s_addc_u32 s33, s33, 0
	global_load_dwordx4 v[248:251], v2, s[32:33] nt
	global_load_dwordx4 v[252:255], v2, s[32:33] offset:16 nt
	s_add_u32 s32, s32, 8192
	s_addc_u32 s33, s33, 0
	global_load_dwordx4 v[84:87], v2, s[34:35] nt
	global_load_dwordx4 v[88:91], v2, s[34:35] offset:16 nt
	s_add_u32 s34, s34, 8192
	s_addc_u32 s35, s35, 0
	global_load_dwordx4 v[92:95], v2, s[34:35] nt
	global_load_dwordx4 v[96:99], v2, s[34:35] offset:16 nt
	s_add_u32 s34, s34, 8192
	s_addc_u32 s35, s35, 0
	global_load_dwordx4 v[100:103], v2, s[34:35] nt
	global_load_dwordx4 v[104:107], v2, s[34:35] offset:16 nt
	s_add_u32 s34, s34, 8192
	s_addc_u32 s35, s35, 0
	global_load_dwordx4 v[108:111], v2, s[34:35] nt
	global_load_dwordx4 v[112:115], v2, s[34:35] offset:16 nt
	s_add_u32 s34, s34, 8192
	s_addc_u32 s35, s35, 0
	global_load_dwordx4 v[116:119], v3, s[40:41] nt
	global_load_dwordx4 v[120:123], v3, s[40:41] offset:16 nt
	s_add_u32 s40, s40, 2048
	s_addc_u32 s41, s41, 0
	global_load_dwordx4 v[124:127], v3, s[40:41] nt
	global_load_dwordx4 v[128:131], v3, s[40:41] offset:16 nt
	s_add_u32 s40, s40, 2048
	s_addc_u32 s41, s41, 0
	global_load_dwordx4 v[132:135], v3, s[40:41] nt
	global_load_dwordx4 v[136:139], v3, s[40:41] offset:16 nt
	s_add_u32 s40, s40, 2048
	s_addc_u32 s41, s41, 0
	global_load_dwordx4 v[140:143], v3, s[40:41] nt
	global_load_dwordx4 v[144:147], v3, s[40:41] offset:16 nt
	s_add_u32 s40, s40, 2048
	s_addc_u32 s41, s41, 0
	global_load_dwordx4 v[148:151], v3, s[40:41] nt
	global_load_dwordx4 v[152:155], v3, s[40:41] offset:16 nt
	s_add_u32 s40, s40, 2048
	s_addc_u32 s41, s41, 0
	global_load_dwordx4 v[156:159], v3, s[40:41] nt
	global_load_dwordx4 v[160:163], v3, s[40:41] offset:16 nt
	s_add_u32 s40, s40, 2048
	s_addc_u32 s41, s41, 0
	global_load_dwordx4 v[164:167], v3, s[40:41] nt
	global_load_dwordx4 v[168:171], v3, s[40:41] offset:16 nt
	s_add_u32 s40, s40, 2048
	s_addc_u32 s41, s41, 0
	global_load_dwordx4 v[172:175], v3, s[40:41] nt
	global_load_dwordx4 v[176:179], v3, s[40:41] offset:16 nt
	s_add_u32 s40, s40, 2048
	s_addc_u32 s41, s41, 0
	s_waitcnt vmcnt(32)
	v_cvt_pk_bf16_f32 v12, v42, v43
	v_cvt_pk_bf16_f32 v13, v44, v45
	v_cvt_pk_bf16_f32 v14, v46, v47
	v_cvt_pk_bf16_f32 v15, v48, v49
	s_mov_b32 s42, 0x0
	buffer_store_dwordx4 v[12:15], v26, s[12:15], s42 offen sc1
	global_load_dwordx4 v[42:45], v3, s[40:41] nt
	global_load_dwordx4 v[46:49], v3, s[40:41] offset:16 nt
	s_add_u32 s40, s40, 2048
	s_addc_u32 s41, s41, 0
	s_waitcnt vmcnt(33)
	v_cvt_pk_bf16_f32 v16, v50, v51
	v_cvt_pk_bf16_f32 v17, v52, v53
	v_cvt_pk_bf16_f32 v18, v54, v55
	v_cvt_pk_bf16_f32 v19, v56, v57
	s_mov_b32 s42, 0x1000
	buffer_store_dwordx4 v[16:19], v26, s[12:15], s42 offen sc1
	global_load_dwordx4 v[50:53], v3, s[40:41] nt
	global_load_dwordx4 v[54:57], v3, s[40:41] offset:16 nt
	s_add_u32 s40, s40, 2048
	s_addc_u32 s41, s41, 0
	s_waitcnt vmcnt(34)
	v_cvt_pk_bf16_f32 v20, v68, v69
	v_cvt_pk_bf16_f32 v21, v70, v71
	v_cvt_pk_bf16_f32 v22, v72, v73
	v_cvt_pk_bf16_f32 v23, v74, v75
	s_mov_b32 s42, 0x2000
	buffer_store_dwordx4 v[20:23], v26, s[12:15], s42 offen sc1
	global_load_dwordx4 v[68:71], v3, s[40:41] nt
	global_load_dwordx4 v[72:75], v3, s[40:41] offset:16 nt
	s_add_u32 s40, s40, 2048
	s_addc_u32 s41, s41, 0
	s_waitcnt vmcnt(35)
	v_cvt_pk_bf16_f32 v12, v76, v77
	v_cvt_pk_bf16_f32 v13, v78, v79
	v_cvt_pk_bf16_f32 v14, v80, v81
	v_cvt_pk_bf16_f32 v15, v82, v83
	s_mov_b32 s42, 0x3000
	buffer_store_dwordx4 v[12:15], v26, s[12:15], s42 offen sc1
	global_load_dwordx4 v[76:79], v3, s[40:41] nt
	global_load_dwordx4 v[80:83], v3, s[40:41] offset:16 nt
	s_add_u32 s40, s40, 2048
	s_addc_u32 s41, s41, 0
	s_waitcnt vmcnt(34)
	v_pk_add_f32 v[200:201], v[84:85], v[200:201]
	v_pk_add_f32 v[202:203], v[86:87], v[202:203]
	v_pk_add_f32 v[204:205], v[88:89], v[204:205]
	v_pk_add_f32 v[206:207], v[90:91], v[206:207]
	v_cvt_pk_bf16_f32 v16, v84, v85
	v_cvt_pk_bf16_f32 v17, v86, v87
	v_cvt_pk_bf16_f32 v18, v88, v89
	v_cvt_pk_bf16_f32 v19, v90, v91
	s_mov_b32 s42, 0x0
	buffer_store_dwordx4 v[16:19], v26, s[4:7], s42 offen sc1
	global_load_dwordx4 v[84:87], v3, s[40:41] nt
	global_load_dwordx4 v[88:91], v3, s[40:41] offset:16 nt
	s_add_u32 s40, s40, 2048
	s_addc_u32 s41, s41, 0
	s_waitcnt vmcnt(35)
	v_pk_add_f32 v[200:201], v[92:93], v[200:201]
	v_pk_add_f32 v[202:203], v[94:95], v[202:203]
	v_pk_add_f32 v[204:205], v[96:97], v[204:205]
	v_pk_add_f32 v[206:207], v[98:99], v[206:207]
	v_cvt_pk_bf16_f32 v20, v92, v93
	v_cvt_pk_bf16_f32 v21, v94, v95
	v_cvt_pk_bf16_f32 v22, v96, v97
	v_cvt_pk_bf16_f32 v23, v98, v99
	s_mov_b32 s42, 0x1000
	buffer_store_dwordx4 v[20:23], v26, s[4:7], s42 offen sc1
	global_load_dwordx4 v[92:95], v3, s[40:41] nt
	global_load_dwordx4 v[96:99], v3, s[40:41] offset:16 nt
	s_add_u32 s40, s40, 2048
	s_addc_u32 s41, s41, 0
	s_waitcnt vmcnt(36)
	v_pk_add_f32 v[200:201], v[100:101], v[200:201]
	v_pk_add_f32 v[202:203], v[102:103], v[202:203]
	v_pk_add_f32 v[204:205], v[104:105], v[204:205]
	v_pk_add_f32 v[206:207], v[106:107], v[206:207]
	v_cvt_pk_bf16_f32 v12, v100, v101
	v_cvt_pk_bf16_f32 v13, v102, v103
	v_cvt_pk_bf16_f32 v14, v104, v105
	v_cvt_pk_bf16_f32 v15, v106, v107
	s_mov_b32 s42, 0x2000
	buffer_store_dwordx4 v[12:15], v26, s[4:7], s42 offen sc1
	global_load_dwordx4 v[100:103], v3, s[40:41] nt
	global_load_dwordx4 v[104:107], v3, s[40:41] offset:16 nt
	s_add_u32 s40, s40, 2048
	s_addc_u32 s41, s41, 0
	s_waitcnt vmcnt(37)
	v_pk_add_f32 v[200:201], v[108:109], v[200:201]
	v_pk_add_f32 v[202:203], v[110:111], v[202:203]
	v_pk_add_f32 v[204:205], v[112:113], v[204:205]
	v_pk_add_f32 v[206:207], v[114:115], v[206:207]
	v_cvt_pk_bf16_f32 v16, v108, v109
	v_cvt_pk_bf16_f32 v17, v110, v111
	v_cvt_pk_bf16_f32 v18, v112, v113
	v_cvt_pk_bf16_f32 v19, v114, v115
	s_mov_b32 s42, 0x3000
	buffer_store_dwordx4 v[16:19], v26, s[4:7], s42 offen sc1
	global_load_dwordx4 v[108:111], v3, s[40:41] nt
	global_load_dwordx4 v[112:115], v3, s[40:41] offset:16 nt
	s_add_u32 s40, s40, 2048
	s_addc_u32 s41, s41, 0
	v_lshrrev_b32_e32 v29, 6, v0
	s_mov_b32 s51, s30
	v_readfirstlane_b32 s50, v29
	s_add_i32 s52, s24, s31
	s_mov_b32 s54, s32
	s_mov_b32 s55, s33
	s_lshl_b32 s43, s30, 16
	s_add_i32 s56, s43, 0x4000
	s_add_u32 s74, s34, 0x10000
	s_addc_u32 s75, s35, 0
	s_mov_b32 s76, s26
	s_mov_b32 s77, s27
	s_add_i32 s61, s28, s43
	s_add_i32 s43, s30, 1
	s_and_b32 s43, s43, 7
	s_lshl_b32 s43, s43, 16
	s_add_i32 s62, s28, s43
	s_add_i32 s43, s30, 2
	s_and_b32 s43, s43, 7
	s_lshl_b32 s43, s43, 16
	s_add_i32 s63, s28, s43
	s_add_i32 s43, s30, 3
	s_and_b32 s43, s43, 7
	s_lshl_b32 s43, s43, 16
	s_add_i32 s87, s28, s43
	s_add_i32 s43, s30, 7
	s_and_b32 s43, s43, 7
	s_lshl_b32 s43, s43, 16
	s_add_i32 s88, s28, s43
	s_add_i32 s88, s88, 0xc000
	s_mov_b32 s58, s87
	s_mov_b32 s57, s63
	s_mov_b32 s59, 0x10000
	s_mov_b32 s60, 0x10000
	s_lshl_b32 s43, s50, 11
	s_add_i32 s84, s43, 0x24000
	s_add_i32 s85, s84, 0x3f0
	s_mov_b32 s64, s10
	s_mov_b32 s65, s11
	s_mov_b32 s66, 0x10000
	s_mov_b32 s67, 0x4000
	s_mov_b32 s68, 0xc000
	s_mov_b32 s69, 0x14000
	s_mov_b32 s70, 0x600df1a6
	s_mov_b32 s71, 0x155510
	s_mov_b32 s72, s46
	s_mov_b32 s73, s47
	s_mov_b32 s53, 0x10000
	v_mov_b32_e32 v208, v2
	v_lshlrev_b32_e32 v41, 2, v39
	v_and_b32_e32 v41, 28, v41
	v_mov_b32_e32 v209, v41
	s_waitcnt vmcnt(0)
	s_barrier
	v_cmp_eq_u32_e32 vcc, 0, v0
	s_and_saveexec_b64 s[38:39], vcc
	s_cbranch_execz .Lpro_noflag
	v_mov_b32_e32 v12, 0x600df1a6
	v_mov_b32_e32 v13, 0
	global_store_dword v13, v12, s[46:47] sc1
.Lpro_noflag:
	s_or_b64 exec, exec, s[38:39]
	v_bfe_u32 v3, v0, 5, 1
	v_lshlrev_b32_e32 v4, 8, v0
	v_and_b32_e32 v4, 0x1f00, v4
	v_and_b32_e32 v5, 7, v0
	v_bitop3_b32 v6, v3, v0, 7 bitop3:0x78
	v_lshl_or_b32 v64, v6, 4, v4
	v_bitop3_b32 v6, v3, v5, 2 bitop3:0x36
	v_lshl_or_b32 v65, v6, 4, v4
	v_bitop3_b32 v6, v3, v5, 4 bitop3:0x36
	v_bitop3_b32 v5, v3, v5, 6 bitop3:0x36
	v_lshl_or_b32 v66, v6, 4, v4
	v_lshl_or_b32 v67, v5, 4, v4
	v_and_b32_e32 v4, 3, v0
	v_lshlrev_b32_e32 v6, 4, v0
	v_lshlrev_b32_e32 v5, 3, v4
	v_and_b32_e32 v6, 0xc0, v6
	v_lshlrev_b32_e32 v8, 1, v0
	v_lshlrev_b32_e32 v9, 8, v3
	v_bfe_u32 v7, v0, 4, 2
	v_and_b32_e32 v8, 32, v8
	v_or3_b32 v5, v5, v9, v6
	s_mov_b32 s0, 0x8000
	v_or3_b32 v184, v5, v8, s0
	v_lshlrev_b32_e32 v5, 8, v7
	v_xor_b32_e32 v6, v7, v1
	s_cmp_lg_u32 0, -1
	v_lshl_or_b32 v222, v6, 4, v5
	v_bitop3_b32 v1, v7, v1, 4 bitop3:0x36
	s_mov_b32 m0, s29
	s_nop 0
	buffer_load_dwordx4 v222, s[12:15], s61 offen lds
	s_cselect_b32 s17, 0, 0
	v_lshl_or_b32 v223, v1, 4, v5
	s_add_i32 s20, s29, 0x400
	s_add_i32 s0, s61, 0x400
	s_mov_b32 m0, s20
	s_nop 0
	buffer_load_dwordx4 v223, s[12:15], s0 offen lds
	v_lshlrev_b32_e32 v0, 6, v0
	s_add_i32 s21, s29, 0x800
	s_add_i32 s0, s61, 0x800
	s_mov_b32 m0, s21
	s_nop 0
	buffer_load_dwordx4 v222, s[12:15], s0 offen lds
	v_and_b32_e32 v0, 0x700, v0
	v_lshlrev_b32_e32 v1, 6, v3
	v_lshlrev_b32_e32 v3, 4, v4
	s_add_i32 s22, s29, 0xc00
	s_add_i32 s1, s61, 0xc00
	s_mov_b32 m0, s22
	s_nop 0
	buffer_load_dwordx4 v223, s[12:15], s1 offen lds
	v_or3_b32 v196, v0, v1, v3
	s_add_i32 s2, s29, 0x8000
	s_mov_b32 m0, s2
	s_nop 0
	buffer_load_dwordx4 v196, s[4:7], s61 offen lds
	s_add_i32 s1, s2, 0x400
	s_add_i32 s3, s61, 0x80
	s_mov_b32 m0, s1
	s_nop 0
	buffer_load_dwordx4 v196, s[4:7], s3 offen lds
	s_add_i32 s1, s2, 0x800
	s_mov_b32 m0, s1
	s_nop 0
	buffer_load_dwordx4 v196, s[4:7], s0 offen lds
	s_add_i32 s0, s2, 0xc00
	s_add_i32 s1, s61, 0x880
	s_mov_b32 m0, s0
	s_nop 0
	buffer_load_dwordx4 v196, s[4:7], s1 offen lds
	v_or_b32_e32 v2, 0x10000, v40
	v_add_u32_e32 v218, s17, v64
	v_add_u32_e32 v219, s17, v65
	v_add_u32_e32 v220, s17, v66
	v_add_u32_e32 v221, s17, v67
	v_add_u32_e32 v32, v2, v218
	v_add_u32_e32 v33, v2, v219
	v_add_u32_e32 v34, v2, v220
	v_add_u32_e32 v35, v2, v221
	v_add_u32_e32 v212, s17, v184
	global_load_dword v38, v41, s[64:65] sc1
	s_mov_b32 m0, s84
	s_nop 0
	buffer_load_dwordx4 v208, s[80:83], s86 offen lds
	s_mov_b32 m0, s85
	s_nop 0
	buffer_load_dwordx4 v208, s[80:83], s86 offen offset:16 lds
	s_add_i32 s86, s86, 0x2000
	v_lshrrev_b32_e32 v37, 4, v39
	v_and_b32_e32 v26, 15, v39
	v_xor_b32_e32 v27, v26, v37
	v_xor_b32_e32 v28, 4, v27
	v_lshlrev_b32_e32 v29, 8, v37
	v_or_b32_e32 v36, 0x10000, v40
	v_add_u32_e32 v29, v29, v36
	v_lshl_add_u32 v24, v27, 4, v29
	v_lshl_add_u32 v25, v28, 4, v29
	v_pk_mul_f32 v[116:117], v[116:117], s[44:45] op_sel_hi:[1,0]
	v_pk_mul_f32 v[118:119], v[118:119], s[44:45] op_sel_hi:[1,0]
	v_pk_mul_f32 v[120:121], v[120:121], s[44:45] op_sel_hi:[1,0]
	v_pk_mul_f32 v[122:123], v[122:123], s[44:45] op_sel_hi:[1,0]
	v_cvt_pk_bf16_f32 v12, v116, v117
	v_cvt_pk_bf16_f32 v13, v118, v119
	v_cvt_pk_bf16_f32 v14, v120, v121
	v_cvt_pk_bf16_f32 v15, v122, v123
	ds_write_b128 v24, v[12:15] offset:0
	v_pk_mul_f32 v[124:125], v[124:125], s[44:45] op_sel_hi:[1,0]
	v_pk_mul_f32 v[126:127], v[126:127], s[44:45] op_sel_hi:[1,0]
	v_pk_mul_f32 v[128:129], v[128:129], s[44:45] op_sel_hi:[1,0]
	v_pk_mul_f32 v[130:131], v[130:131], s[44:45] op_sel_hi:[1,0]
	v_cvt_pk_bf16_f32 v16, v124, v125
	v_cvt_pk_bf16_f32 v17, v126, v127
	v_cvt_pk_bf16_f32 v18, v128, v129
	v_cvt_pk_bf16_f32 v19, v130, v131
	ds_write_b128 v25, v[16:19] offset:1024
	v_pk_mul_f32 v[132:133], v[132:133], s[44:45] op_sel_hi:[1,0]
	v_pk_mul_f32 v[134:135], v[134:135], s[44:45] op_sel_hi:[1,0]
	v_pk_mul_f32 v[136:137], v[136:137], s[44:45] op_sel_hi:[1,0]
	v_pk_mul_f32 v[138:139], v[138:139], s[44:45] op_sel_hi:[1,0]
	v_cvt_pk_bf16_f32 v20, v132, v133
	v_cvt_pk_bf16_f32 v21, v134, v135
	v_cvt_pk_bf16_f32 v22, v136, v137
	v_cvt_pk_bf16_f32 v23, v138, v139
	ds_write_b128 v24, v[20:23] offset:2048
	v_pk_mul_f32 v[140:141], v[140:141], s[44:45] op_sel_hi:[1,0]
	v_pk_mul_f32 v[142:143], v[142:143], s[44:45] op_sel_hi:[1,0]
	v_pk_mul_f32 v[144:145], v[144:145], s[44:45] op_sel_hi:[1,0]
	v_pk_mul_f32 v[146:147], v[146:147], s[44:45] op_sel_hi:[1,0]
	v_cvt_pk_bf16_f32 v12, v140, v141
	v_cvt_pk_bf16_f32 v13, v142, v143
	v_cvt_pk_bf16_f32 v14, v144, v145
	v_cvt_pk_bf16_f32 v15, v146, v147
	ds_write_b128 v25, v[12:15] offset:3072
	v_pk_mul_f32 v[148:149], v[148:149], s[44:45] op_sel_hi:[1,0]
	v_pk_mul_f32 v[150:151], v[150:151], s[44:45] op_sel_hi:[1,0]
	v_pk_mul_f32 v[152:153], v[152:153], s[44:45] op_sel_hi:[1,0]
	v_pk_mul_f32 v[154:155], v[154:155], s[44:45] op_sel_hi:[1,0]
	v_cvt_pk_bf16_f32 v16, v148, v149
	v_cvt_pk_bf16_f32 v17, v150, v151
	v_cvt_pk_bf16_f32 v18, v152, v153
	v_cvt_pk_bf16_f32 v19, v154, v155
	ds_write_b128 v24, v[16:19] offset:4096
	v_pk_mul_f32 v[156:157], v[156:157], s[44:45] op_sel_hi:[1,0]
	v_pk_mul_f32 v[158:159], v[158:159], s[44:45] op_sel_hi:[1,0]
	v_pk_mul_f32 v[160:161], v[160:161], s[44:45] op_sel_hi:[1,0]
	v_pk_mul_f32 v[162:163], v[162:163], s[44:45] op_sel_hi:[1,0]
	v_cvt_pk_bf16_f32 v20, v156, v157
	v_cvt_pk_bf16_f32 v21, v158, v159
	v_cvt_pk_bf16_f32 v22, v160, v161
	v_cvt_pk_bf16_f32 v23, v162, v163
	ds_write_b128 v25, v[20:23] offset:5120
	v_pk_mul_f32 v[164:165], v[164:165], s[44:45] op_sel_hi:[1,0]
	v_pk_mul_f32 v[166:167], v[166:167], s[44:45] op_sel_hi:[1,0]
	v_pk_mul_f32 v[168:169], v[168:169], s[44:45] op_sel_hi:[1,0]
	v_pk_mul_f32 v[170:171], v[170:171], s[44:45] op_sel_hi:[1,0]
	v_cvt_pk_bf16_f32 v12, v164, v165
	v_cvt_pk_bf16_f32 v13, v166, v167
	v_cvt_pk_bf16_f32 v14, v168, v169
	v_cvt_pk_bf16_f32 v15, v170, v171
	ds_write_b128 v24, v[12:15] offset:6144
	v_pk_mul_f32 v[172:173], v[172:173], s[44:45] op_sel_hi:[1,0]
	v_pk_mul_f32 v[174:175], v[174:175], s[44:45] op_sel_hi:[1,0]
	v_pk_mul_f32 v[176:177], v[176:177], s[44:45] op_sel_hi:[1,0]
	v_pk_mul_f32 v[178:179], v[178:179], s[44:45] op_sel_hi:[1,0]
	v_cvt_pk_bf16_f32 v16, v172, v173
	v_cvt_pk_bf16_f32 v17, v174, v175
	v_cvt_pk_bf16_f32 v18, v176, v177
	v_cvt_pk_bf16_f32 v19, v178, v179
	ds_write_b128 v25, v[16:19] offset:7168
	v_pk_mul_f32 v[42:43], v[42:43], s[44:45] op_sel_hi:[1,0]
	v_pk_mul_f32 v[44:45], v[44:45], s[44:45] op_sel_hi:[1,0]
	v_pk_mul_f32 v[46:47], v[46:47], s[44:45] op_sel_hi:[1,0]
	v_pk_mul_f32 v[48:49], v[48:49], s[44:45] op_sel_hi:[1,0]
	v_cvt_pk_bf16_f32 v20, v42, v43
	v_cvt_pk_bf16_f32 v21, v44, v45
	v_cvt_pk_bf16_f32 v22, v46, v47
	v_cvt_pk_bf16_f32 v23, v48, v49
	ds_write_b128 v24, v[20:23] offset:8192
	v_pk_mul_f32 v[50:51], v[50:51], s[44:45] op_sel_hi:[1,0]
	v_pk_mul_f32 v[52:53], v[52:53], s[44:45] op_sel_hi:[1,0]
	v_pk_mul_f32 v[54:55], v[54:55], s[44:45] op_sel_hi:[1,0]
	v_pk_mul_f32 v[56:57], v[56:57], s[44:45] op_sel_hi:[1,0]
	v_cvt_pk_bf16_f32 v12, v50, v51
	v_cvt_pk_bf16_f32 v13, v52, v53
	v_cvt_pk_bf16_f32 v14, v54, v55
	v_cvt_pk_bf16_f32 v15, v56, v57
	ds_write_b128 v25, v[12:15] offset:9216
	v_pk_mul_f32 v[68:69], v[68:69], s[44:45] op_sel_hi:[1,0]
	v_pk_mul_f32 v[70:71], v[70:71], s[44:45] op_sel_hi:[1,0]
	v_pk_mul_f32 v[72:73], v[72:73], s[44:45] op_sel_hi:[1,0]
	v_pk_mul_f32 v[74:75], v[74:75], s[44:45] op_sel_hi:[1,0]
	v_cvt_pk_bf16_f32 v16, v68, v69
	v_cvt_pk_bf16_f32 v17, v70, v71
	v_cvt_pk_bf16_f32 v18, v72, v73
	v_cvt_pk_bf16_f32 v19, v74, v75
	ds_write_b128 v24, v[16:19] offset:10240
	v_pk_mul_f32 v[76:77], v[76:77], s[44:45] op_sel_hi:[1,0]
	v_pk_mul_f32 v[78:79], v[78:79], s[44:45] op_sel_hi:[1,0]
	v_pk_mul_f32 v[80:81], v[80:81], s[44:45] op_sel_hi:[1,0]
	v_pk_mul_f32 v[82:83], v[82:83], s[44:45] op_sel_hi:[1,0]
	v_cvt_pk_bf16_f32 v20, v76, v77
	v_cvt_pk_bf16_f32 v21, v78, v79
	v_cvt_pk_bf16_f32 v22, v80, v81
	v_cvt_pk_bf16_f32 v23, v82, v83
	ds_write_b128 v25, v[20:23] offset:11264
	v_pk_mul_f32 v[84:85], v[84:85], s[44:45] op_sel_hi:[1,0]
	v_pk_mul_f32 v[86:87], v[86:87], s[44:45] op_sel_hi:[1,0]
	v_pk_mul_f32 v[88:89], v[88:89], s[44:45] op_sel_hi:[1,0]
	v_pk_mul_f32 v[90:91], v[90:91], s[44:45] op_sel_hi:[1,0]
	v_cvt_pk_bf16_f32 v12, v84, v85
	v_cvt_pk_bf16_f32 v13, v86, v87
	v_cvt_pk_bf16_f32 v14, v88, v89
	v_cvt_pk_bf16_f32 v15, v90, v91
	ds_write_b128 v24, v[12:15] offset:12288
	v_pk_mul_f32 v[92:93], v[92:93], s[44:45] op_sel_hi:[1,0]
	v_pk_mul_f32 v[94:95], v[94:95], s[44:45] op_sel_hi:[1,0]
	v_pk_mul_f32 v[96:97], v[96:97], s[44:45] op_sel_hi:[1,0]
	v_pk_mul_f32 v[98:99], v[98:99], s[44:45] op_sel_hi:[1,0]
	v_cvt_pk_bf16_f32 v16, v92, v93
	v_cvt_pk_bf16_f32 v17, v94, v95
	v_cvt_pk_bf16_f32 v18, v96, v97
	v_cvt_pk_bf16_f32 v19, v98, v99
	ds_write_b128 v25, v[16:19] offset:13312
	v_pk_mul_f32 v[100:101], v[100:101], s[44:45] op_sel_hi:[1,0]
	v_pk_mul_f32 v[102:103], v[102:103], s[44:45] op_sel_hi:[1,0]
	v_pk_mul_f32 v[104:105], v[104:105], s[44:45] op_sel_hi:[1,0]
	v_pk_mul_f32 v[106:107], v[106:107], s[44:45] op_sel_hi:[1,0]
	v_cvt_pk_bf16_f32 v20, v100, v101
	v_cvt_pk_bf16_f32 v21, v102, v103
	v_cvt_pk_bf16_f32 v22, v104, v105
	v_cvt_pk_bf16_f32 v23, v106, v107
	ds_write_b128 v24, v[20:23] offset:14336
	v_pk_mul_f32 v[108:109], v[108:109], s[44:45] op_sel_hi:[1,0]
	v_pk_mul_f32 v[110:111], v[110:111], s[44:45] op_sel_hi:[1,0]
	v_pk_mul_f32 v[112:113], v[112:113], s[44:45] op_sel_hi:[1,0]
	v_pk_mul_f32 v[114:115], v[114:115], s[44:45] op_sel_hi:[1,0]
	v_cvt_pk_bf16_f32 v12, v108, v109
	v_cvt_pk_bf16_f32 v13, v110, v111
	v_cvt_pk_bf16_f32 v14, v112, v113
	v_cvt_pk_bf16_f32 v15, v114, v115
	ds_write_b128 v25, v[12:15] offset:15360
	s_waitcnt lgkmcnt(0)
	ds_read_b128 v[0:3], v32 offset:0
	ds_read_b128 v[4:7], v33 offset:0
	ds_read_b128 v[8:11], v34 offset:0
	ds_read_b128 v[12:15], v35 offset:0
	ds_read_b128 v[16:19], v32 offset:128
	ds_read_b128 v[20:23], v33 offset:128
	ds_read_b128 v[24:27], v34 offset:128
	ds_read_b128 v[28:31], v35 offset:128
	s_waitcnt lgkmcnt(0)
	v_accvgpr_write_b32 a[128], v0
	v_accvgpr_write_b32 a[129], v1
	v_accvgpr_write_b32 a[130], v2
	v_accvgpr_write_b32 a[131], v3
	v_accvgpr_write_b32 a[132], v4
	v_accvgpr_write_b32 a[133], v5
	v_accvgpr_write_b32 a[134], v6
	v_accvgpr_write_b32 a[135], v7
	v_accvgpr_write_b32 a[136], v8
	v_accvgpr_write_b32 a[137], v9
	v_accvgpr_write_b32 a[138], v10
	v_accvgpr_write_b32 a[139], v11
	v_accvgpr_write_b32 a[140], v12
	v_accvgpr_write_b32 a[141], v13
	v_accvgpr_write_b32 a[142], v14
	v_accvgpr_write_b32 a[143], v15
	v_accvgpr_write_b32 a[144], v16
	v_accvgpr_write_b32 a[145], v17
	v_accvgpr_write_b32 a[146], v18
	v_accvgpr_write_b32 a[147], v19
	v_accvgpr_write_b32 a[148], v20
	v_accvgpr_write_b32 a[149], v21
	v_accvgpr_write_b32 a[150], v22
	v_accvgpr_write_b32 a[151], v23
	v_accvgpr_write_b32 a[152], v24
	v_accvgpr_write_b32 a[153], v25
	v_accvgpr_write_b32 a[154], v26
	v_accvgpr_write_b32 a[155], v27
	v_accvgpr_write_b32 a[156], v28
	v_accvgpr_write_b32 a[157], v29
	v_accvgpr_write_b32 a[158], v30
	v_accvgpr_write_b32 a[159], v31
	ds_read_b128 v[0:3], v32 offset:8192
	ds_read_b128 v[4:7], v33 offset:8192
	ds_read_b128 v[8:11], v34 offset:8192
	ds_read_b128 v[12:15], v35 offset:8192
	ds_read_b128 v[16:19], v32 offset:8320
	ds_read_b128 v[20:23], v33 offset:8320
	ds_read_b128 v[24:27], v34 offset:8320
	ds_read_b128 v[28:31], v35 offset:8320
	s_waitcnt lgkmcnt(0)
	v_accvgpr_write_b32 a[160], v0
	v_accvgpr_write_b32 a[161], v1
	v_accvgpr_write_b32 a[162], v2
	v_accvgpr_write_b32 a[163], v3
	v_accvgpr_write_b32 a[164], v4
	v_accvgpr_write_b32 a[165], v5
	v_accvgpr_write_b32 a[166], v6
	v_accvgpr_write_b32 a[167], v7
	v_accvgpr_write_b32 a[168], v8
	v_accvgpr_write_b32 a[169], v9
	v_accvgpr_write_b32 a[170], v10
	v_accvgpr_write_b32 a[171], v11
	v_accvgpr_write_b32 a[172], v12
	v_accvgpr_write_b32 a[173], v13
	v_accvgpr_write_b32 a[174], v14
	v_accvgpr_write_b32 a[175], v15
	v_accvgpr_write_b32 a[176], v16
	v_accvgpr_write_b32 a[177], v17
	v_accvgpr_write_b32 a[178], v18
	v_accvgpr_write_b32 a[179], v19
	v_accvgpr_write_b32 a[180], v20
	v_accvgpr_write_b32 a[181], v21
	v_accvgpr_write_b32 a[182], v22
	v_accvgpr_write_b32 a[183], v23
	v_accvgpr_write_b32 a[184], v24
	v_accvgpr_write_b32 a[185], v25
	v_accvgpr_write_b32 a[186], v26
	v_accvgpr_write_b32 a[187], v27
	v_accvgpr_write_b32 a[188], v28
	v_accvgpr_write_b32 a[189], v29
	v_accvgpr_write_b32 a[190], v30
	v_accvgpr_write_b32 a[191], v31
	s_waitcnt vmcnt(0) lgkmcnt(0)
	s_barrier
	s_nop 0
	ds_read_b128 a[192:195], v218 offset:0
	s_nop 0
	ds_read_b128 a[196:199], v219 offset:0
	ds_read_b128 a[200:203], v220 offset:0
	ds_read_b128 a[204:207], v221 offset:0
	ds_read_b128 a[208:211], v218 offset:128
	ds_read_b128 a[212:215], v219 offset:128
	ds_read_b128 a[216:219], v220 offset:128
	ds_read_b128 a[220:223], v221 offset:128
	ds_read_b128 a[224:227], v218 offset:8192
	ds_read_b128 a[228:231], v219 offset:8192
	ds_read_b128 a[232:235], v220 offset:8192
	ds_read_b128 a[236:239], v221 offset:8192
	ds_read_b128 a[240:243], v218 offset:8320
	ds_read_b128 a[244:247], v219 offset:8320
	ds_read_b128 a[248:251], v220 offset:8320
	ds_read_b128 a[252:255], v221 offset:8320
	s_waitcnt lgkmcnt(0)
	s_nop 0
	s_waitcnt vmcnt(0)
	v_cmp_eq_u32_e32 vcc, s70, v38
	s_cmp_eq_u64 vcc, exec
	s_cbranch_scc0 .LBB0_27
